# v26 + RG-LRU pass-2 prologue (walk of 128 chunk summaries per channel) rewritten by hand with 8 loads in flight instead of 2
# speedup vs baseline: 1.0078x; 1.0078x over previous
; template <bool FINAL> __device__ __forceinline__ void rglru_pass(Frame& F) {
;     ...
;     if (FINAL) { const int b = F.tid >> 8, zz = (F.tid >> 7) & 1, cl = F.tid & 127; const float* sb = SUM + ((size_t)zz * DM + h * 128 + cl) * 2;
;         float s = 0.f;
; #pragma unroll
;         for (int i = 0; i < 4; ++i) { const int c = 256 + b * 4 + (zz ? 3 - i : i); const float2 ab = *(const float2*)(sb + (size_t)c * 4 * DM); s = ab.x * s + ab.y; }
; #pragma unroll 8
;         for (int i = 0; i < 128; ++i) { const int c = b * 128 + (zz ? 127 - i : i); const float2 ab = *(const float2*)(sb + (size_t)c * 4 * DM);
;             const int d = c - cg; if (d >= 0 && d % ncg == 0) CL[(d / ncg) * 256 + zz * 128 + cl] = s;
;             s = ab.x * s + ab.y; }
;         __syncthreads(); }
.LBB0_1548:
	s_or_b64 exec, exec, s[12:13]
	v_bfe_u32 v27, v180, 7, 1
	v_ashrrev_i32_e32 v26, 8, v180
	v_lshlrev_b32_e32 v4, 11, v27
	v_or3_b32 v4, v4, s23, v12
	v_lshlrev_b32_e32 v22, 2, v26
	v_lshlrev_b32_e32 v4, 1, v4
	v_mov_b32_e32 v5, 0
	v_add_u32_e32 v24, 0x100, v22
	v_sub_u32_e32 v22, v22, v27
	v_lshl_add_u64 v[4:5], v[4:5], 2, s[88:89]
	s_mov_b64 s[0:1], 0x300000
	v_ashrrev_i32_e32 v23, 31, v22
	v_lshl_add_u64 v[4:5], v[4:5], 0, s[0:1]
	v_lshlrev_b64 v[22:23], 15, v[22:23]
	v_lshl_add_u64 v[22:23], v[4:5], 0, v[22:23]
	s_mov_b32 s0, 0x810000
	v_add_co_u32_e32 v22, vcc, s0, v22
	v_bfe_i32 v1, v180, 7, 1
	s_nop 0
	v_addc_co_u32_e32 v23, vcc, 0, v23, vcc
	v_and_or_b32 v6, v1, 3, v24
	v_or_b32_e32 v1, v27, v24
	v_cmp_eq_u32_e32 vcc, 0, v27
	v_add_u32_e32 v8, 1, v1
	v_ashrrev_i32_e32 v7, 31, v6
	v_cndmask_b32_e64 v1, 0, 3, vcc
	v_ashrrev_i32_e32 v9, 31, v8
	v_or_b32_e32 v24, v1, v24
	v_lshlrev_b64 v[6:7], 15, v[6:7]
	v_lshlrev_b64 v[8:9], 15, v[8:9]
	v_ashrrev_i32_e32 v25, 31, v24
	v_lshl_add_u64 v[6:7], v[4:5], 0, v[6:7]
	v_lshl_add_u64 v[8:9], v[4:5], 0, v[8:9]
	v_lshlrev_b64 v[24:25], 15, v[24:25]
	s_waitcnt lgkmcnt(0)
	s_barrier
	v_lshl_add_u64 v[24:25], v[4:5], 0, v[24:25]
	global_load_dwordx2 v[28:29], v[6:7], off
	s_nop 0
	global_load_dwordx2 v[8:9], v[8:9], off
	s_nop 0
	global_load_dwordx2 v[30:31], v[22:23], off
	global_load_dwordx2 v[6:7], v[24:25], off
	s_abs_i32 s13, s21
	v_fmac_f32_e32 v20, v19, v10
	v_cvt_f32_u32_e32 v10, s13
	v_fmac_f32_e32 v21, 0xb102e308, v11
	s_add_i32 s0, 0, 0x1ce00
	s_sub_i32 s4, 0, s13
	v_rcp_iflag_f32_e32 v35, v10
	v_lshlrev_b32_e32 v10, 2, v12
	v_lshlrev_b32_e32 v12, 9, v27
	v_add3_u32 v25, s0, v12, v10
	v_mul_f32_e32 v11, 0x4f7ffffe, v35
	v_cvt_u32_f32_e32 v11, v11
	v_ldexp_f32 v23, v17, 1
	v_ldexp_f32 v22, v13, 1
	v_and_b32_e32 v1, 0x7fffffff, v15
	v_mul_lo_u32 v10, s4, v11
	v_mul_hi_u32 v10, v11, v10
	s_mov_b32 s6, 0
	s_ashr_i32 s14, s21, 31
	v_lshlrev_b32_e32 v24, 7, v26
	v_add_u32_e32 v26, v11, v10
	s_movk_i32 s5, 0x78
	s_waitcnt vmcnt(3)
	v_fmac_f32_e32 v29, 0, v28
	s_waitcnt vmcnt(2)
	v_fmac_f32_e32 v9, v29, v8
	s_waitcnt vmcnt(1)
	v_fmac_f32_e32 v31, v9, v30
	s_waitcnt vmcnt(0)
	v_fmac_f32_e32 v7, v31, v6
	v_mov_b32_e32 v6, 1
	v_mov_b32_e32 v8, -1
	v_cndmask_b32_e32 v6, v8, v6, vcc
	v_mov_b32_e32 v8, 0
	v_mov_b32_e32 v9, 0x7f
	v_cndmask_b32_e32 v8, v9, v8, vcc
	v_add_u32_e32 v227, v24, v8
	v_mov_b32_e32 v8, v227
	v_mov_b32_e32 v9, 0
	v_lshlrev_b64 v[244:245], 15, v[8:9]
	v_lshl_add_u64 v[244:245], v[4:5], 0, v[244:245]
	v_lshlrev_b32_e32 v246, 15, v6
	v_ashrrev_i32_e32 v247, 31, v6
	global_load_dwordx2 v[228:229], v[244:245], off
	v_lshl_add_u64 v[244:245], v[244:245], 0, v[246:247]
	global_load_dwordx2 v[230:231], v[244:245], off
	v_lshl_add_u64 v[244:245], v[244:245], 0, v[246:247]
	global_load_dwordx2 v[232:233], v[244:245], off
	v_lshl_add_u64 v[244:245], v[244:245], 0, v[246:247]
	global_load_dwordx2 v[234:235], v[244:245], off
	v_lshl_add_u64 v[244:245], v[244:245], 0, v[246:247]
	global_load_dwordx2 v[236:237], v[244:245], off
	v_lshl_add_u64 v[244:245], v[244:245], 0, v[246:247]
	global_load_dwordx2 v[238:239], v[244:245], off
	v_lshl_add_u64 v[244:245], v[244:245], 0, v[246:247]
	global_load_dwordx2 v[240:241], v[244:245], off
	v_lshl_add_u64 v[244:245], v[244:245], 0, v[246:247]
	global_load_dwordx2 v[242:243], v[244:245], off
	v_lshl_add_u64 v[244:245], v[244:245], 0, v[246:247]
	s_movk_i32 s5, 16
.Lwalk13:
	s_waitcnt vmcnt(7)
	v_subrev_u32_e32 v9, s20, v227
	v_sub_u32_e32 v10, 0, v9
	v_max_i32_e32 v10, v9, v10
	v_mul_hi_u32 v12, v10, v26
	v_mul_lo_u32 v13, v12, s13
	v_sub_u32_e32 v10, v10, v13
	v_add_u32_e32 v13, 1, v12
	v_cmp_le_u32_e64 s[2:3], s13, v10
	v_ashrrev_i32_e32 v8, 31, v9
	v_xor_b32_e32 v8, s14, v8
	v_cndmask_b32_e64 v12, v12, v13, s[2:3]
	v_subrev_u32_e32 v13, s13, v10
	v_cndmask_b32_e64 v10, v10, v13, s[2:3]
	v_add_u32_e32 v13, 1, v12
	v_cmp_le_u32_e64 s[2:3], s13, v10
	v_cmp_lt_i32_e64 s[0:1], -1, v9
	s_nop 0
	v_cndmask_b32_e64 v10, v12, v13, s[2:3]
	v_xor_b32_e32 v10, v10, v8
	v_sub_u32_e32 v8, v10, v8
	v_mul_lo_u32 v10, v8, s21
	v_sub_u32_e32 v9, v9, v10
	v_cmp_eq_u32_e64 s[2:3], 0, v9
	s_and_b64 s[2:3], s[0:1], s[2:3]
	s_and_saveexec_b64 s[0:1], s[2:3]
	s_cbranch_execz .Lwalk13_s0
	v_lshl_add_u32 v8, v8, 10, v25
	ds_write_b32 v8, v7
.Lwalk13_s0:
	s_or_b64 exec, exec, s[0:1]
	v_fma_f32 v7, v228, v7, v229
	v_add_u32_e32 v227, v227, v6
	global_load_dwordx2 v[228:229], v[244:245], off
	v_lshl_add_u64 v[244:245], v[244:245], 0, v[246:247]
	s_waitcnt vmcnt(7)
	v_subrev_u32_e32 v9, s20, v227
	v_sub_u32_e32 v10, 0, v9
	v_max_i32_e32 v10, v9, v10
	v_mul_hi_u32 v12, v10, v26
	v_mul_lo_u32 v13, v12, s13
	v_sub_u32_e32 v10, v10, v13
	v_add_u32_e32 v13, 1, v12
	v_cmp_le_u32_e64 s[2:3], s13, v10
	v_ashrrev_i32_e32 v8, 31, v9
	v_xor_b32_e32 v8, s14, v8
	v_cndmask_b32_e64 v12, v12, v13, s[2:3]
	v_subrev_u32_e32 v13, s13, v10
	v_cndmask_b32_e64 v10, v10, v13, s[2:3]
	v_add_u32_e32 v13, 1, v12
	v_cmp_le_u32_e64 s[2:3], s13, v10
	v_cmp_lt_i32_e64 s[0:1], -1, v9
	s_nop 0
	v_cndmask_b32_e64 v10, v12, v13, s[2:3]
	v_xor_b32_e32 v10, v10, v8
	v_sub_u32_e32 v8, v10, v8
	v_mul_lo_u32 v10, v8, s21
	v_sub_u32_e32 v9, v9, v10
	v_cmp_eq_u32_e64 s[2:3], 0, v9
	s_and_b64 s[2:3], s[0:1], s[2:3]
	s_and_saveexec_b64 s[0:1], s[2:3]
	s_cbranch_execz .Lwalk13_s1
	v_lshl_add_u32 v8, v8, 10, v25
	ds_write_b32 v8, v7
; template <bool FINAL> __device__ __forceinline__ void rglru_pass(Frame& F) {
;     ...
;         for (int i = 0; i < 128; ++i) { const int c = b * 128 + (zz ? 127 - i : i); const float2 ab = *(const float2*)(sb + (size_t)c * 4 * DM);
;             const int d = c - cg; if (d >= 0 && d % ncg == 0) CL[(d / ncg) * 256 + zz * 128 + cl] = s;
;             s = ab.x * s + ab.y; }
;         __syncthreads(); }
.Lwalk13_s1:
	s_or_b64 exec, exec, s[0:1]
	v_fma_f32 v7, v230, v7, v231
	v_add_u32_e32 v227, v227, v6
	global_load_dwordx2 v[230:231], v[244:245], off
	v_lshl_add_u64 v[244:245], v[244:245], 0, v[246:247]
	s_waitcnt vmcnt(7)
	v_subrev_u32_e32 v9, s20, v227
	v_sub_u32_e32 v10, 0, v9
	v_max_i32_e32 v10, v9, v10
	v_mul_hi_u32 v12, v10, v26
	v_mul_lo_u32 v13, v12, s13
	v_sub_u32_e32 v10, v10, v13
	v_add_u32_e32 v13, 1, v12
	v_cmp_le_u32_e64 s[2:3], s13, v10
	v_ashrrev_i32_e32 v8, 31, v9
	v_xor_b32_e32 v8, s14, v8
	v_cndmask_b32_e64 v12, v12, v13, s[2:3]
	v_subrev_u32_e32 v13, s13, v10
	v_cndmask_b32_e64 v10, v10, v13, s[2:3]
	v_add_u32_e32 v13, 1, v12
	v_cmp_le_u32_e64 s[2:3], s13, v10
	v_cmp_lt_i32_e64 s[0:1], -1, v9
	s_nop 0
	v_cndmask_b32_e64 v10, v12, v13, s[2:3]
	v_xor_b32_e32 v10, v10, v8
	v_sub_u32_e32 v8, v10, v8
	v_mul_lo_u32 v10, v8, s21
	v_sub_u32_e32 v9, v9, v10
	v_cmp_eq_u32_e64 s[2:3], 0, v9
	s_and_b64 s[2:3], s[0:1], s[2:3]
	s_and_saveexec_b64 s[0:1], s[2:3]
	s_cbranch_execz .Lwalk13_s2
	v_lshl_add_u32 v8, v8, 10, v25
	ds_write_b32 v8, v7
.Lwalk13_s2:
	s_or_b64 exec, exec, s[0:1]
	v_fma_f32 v7, v232, v7, v233
	v_add_u32_e32 v227, v227, v6
	global_load_dwordx2 v[232:233], v[244:245], off
	v_lshl_add_u64 v[244:245], v[244:245], 0, v[246:247]
	s_waitcnt vmcnt(7)
	v_subrev_u32_e32 v9, s20, v227
	v_sub_u32_e32 v10, 0, v9
	v_max_i32_e32 v10, v9, v10
	v_mul_hi_u32 v12, v10, v26
	v_mul_lo_u32 v13, v12, s13
	v_sub_u32_e32 v10, v10, v13
	v_add_u32_e32 v13, 1, v12
	v_cmp_le_u32_e64 s[2:3], s13, v10
	v_ashrrev_i32_e32 v8, 31, v9
	v_xor_b32_e32 v8, s14, v8
	v_cndmask_b32_e64 v12, v12, v13, s[2:3]
	v_subrev_u32_e32 v13, s13, v10
	v_cndmask_b32_e64 v10, v10, v13, s[2:3]
	v_add_u32_e32 v13, 1, v12
	v_cmp_le_u32_e64 s[2:3], s13, v10
	v_cmp_lt_i32_e64 s[0:1], -1, v9
	s_nop 0
	v_cndmask_b32_e64 v10, v12, v13, s[2:3]
	v_xor_b32_e32 v10, v10, v8
	v_sub_u32_e32 v8, v10, v8
	v_mul_lo_u32 v10, v8, s21
	v_sub_u32_e32 v9, v9, v10
	v_cmp_eq_u32_e64 s[2:3], 0, v9
	s_and_b64 s[2:3], s[0:1], s[2:3]
	s_and_saveexec_b64 s[0:1], s[2:3]
	s_cbranch_execz .Lwalk13_s3
	v_lshl_add_u32 v8, v8, 10, v25
	ds_write_b32 v8, v7
.Lwalk13_s3:
	s_or_b64 exec, exec, s[0:1]
	v_fma_f32 v7, v234, v7, v235
	v_add_u32_e32 v227, v227, v6
	global_load_dwordx2 v[234:235], v[244:245], off
	v_lshl_add_u64 v[244:245], v[244:245], 0, v[246:247]
	s_waitcnt vmcnt(7)
	v_subrev_u32_e32 v9, s20, v227
	v_sub_u32_e32 v10, 0, v9
	v_max_i32_e32 v10, v9, v10
	v_mul_hi_u32 v12, v10, v26
	v_mul_lo_u32 v13, v12, s13
	v_sub_u32_e32 v10, v10, v13
	v_add_u32_e32 v13, 1, v12
	v_cmp_le_u32_e64 s[2:3], s13, v10
	v_ashrrev_i32_e32 v8, 31, v9
	v_xor_b32_e32 v8, s14, v8
	v_cndmask_b32_e64 v12, v12, v13, s[2:3]
	v_subrev_u32_e32 v13, s13, v10
	v_cndmask_b32_e64 v10, v10, v13, s[2:3]
	v_add_u32_e32 v13, 1, v12
	v_cmp_le_u32_e64 s[2:3], s13, v10
	v_cmp_lt_i32_e64 s[0:1], -1, v9
	s_nop 0
	v_cndmask_b32_e64 v10, v12, v13, s[2:3]
	v_xor_b32_e32 v10, v10, v8
	v_sub_u32_e32 v8, v10, v8
	v_mul_lo_u32 v10, v8, s21
	v_sub_u32_e32 v9, v9, v10
	v_cmp_eq_u32_e64 s[2:3], 0, v9
	s_and_b64 s[2:3], s[0:1], s[2:3]
	s_and_saveexec_b64 s[0:1], s[2:3]
	s_cbranch_execz .Lwalk13_s4
	v_lshl_add_u32 v8, v8, 10, v25
	ds_write_b32 v8, v7
.Lwalk13_s4:
	s_or_b64 exec, exec, s[0:1]
	v_fma_f32 v7, v236, v7, v237
	v_add_u32_e32 v227, v227, v6
	global_load_dwordx2 v[236:237], v[244:245], off
	v_lshl_add_u64 v[244:245], v[244:245], 0, v[246:247]
	s_waitcnt vmcnt(7)
	v_subrev_u32_e32 v9, s20, v227
	v_sub_u32_e32 v10, 0, v9
	v_max_i32_e32 v10, v9, v10
	v_mul_hi_u32 v12, v10, v26
	v_mul_lo_u32 v13, v12, s13
	v_sub_u32_e32 v10, v10, v13
	v_add_u32_e32 v13, 1, v12
	v_cmp_le_u32_e64 s[2:3], s13, v10
	v_ashrrev_i32_e32 v8, 31, v9
	v_xor_b32_e32 v8, s14, v8
	v_cndmask_b32_e64 v12, v12, v13, s[2:3]
	v_subrev_u32_e32 v13, s13, v10
	v_cndmask_b32_e64 v10, v10, v13, s[2:3]
	v_add_u32_e32 v13, 1, v12
	v_cmp_le_u32_e64 s[2:3], s13, v10
	v_cmp_lt_i32_e64 s[0:1], -1, v9
	s_nop 0
	v_cndmask_b32_e64 v10, v12, v13, s[2:3]
	v_xor_b32_e32 v10, v10, v8
	v_sub_u32_e32 v8, v10, v8
	v_mul_lo_u32 v10, v8, s21
	v_sub_u32_e32 v9, v9, v10
	v_cmp_eq_u32_e64 s[2:3], 0, v9
	s_and_b64 s[2:3], s[0:1], s[2:3]
	s_and_saveexec_b64 s[0:1], s[2:3]
	s_cbranch_execz .Lwalk13_s5
	v_lshl_add_u32 v8, v8, 10, v25
	ds_write_b32 v8, v7
.Lwalk13_s5:
	s_or_b64 exec, exec, s[0:1]
	v_fma_f32 v7, v238, v7, v239
	v_add_u32_e32 v227, v227, v6
	global_load_dwordx2 v[238:239], v[244:245], off
	v_lshl_add_u64 v[244:245], v[244:245], 0, v[246:247]
	s_waitcnt vmcnt(7)
	v_subrev_u32_e32 v9, s20, v227
	v_sub_u32_e32 v10, 0, v9
	v_max_i32_e32 v10, v9, v10
	v_mul_hi_u32 v12, v10, v26
	v_mul_lo_u32 v13, v12, s13
	v_sub_u32_e32 v10, v10, v13
	v_add_u32_e32 v13, 1, v12
	v_cmp_le_u32_e64 s[2:3], s13, v10
	v_ashrrev_i32_e32 v8, 31, v9
	v_xor_b32_e32 v8, s14, v8
	v_cndmask_b32_e64 v12, v12, v13, s[2:3]
	v_subrev_u32_e32 v13, s13, v10
	v_cndmask_b32_e64 v10, v10, v13, s[2:3]
	v_add_u32_e32 v13, 1, v12
	v_cmp_le_u32_e64 s[2:3], s13, v10
	v_cmp_lt_i32_e64 s[0:1], -1, v9
	s_nop 0
	v_cndmask_b32_e64 v10, v12, v13, s[2:3]
	v_xor_b32_e32 v10, v10, v8
	v_sub_u32_e32 v8, v10, v8
	v_mul_lo_u32 v10, v8, s21
	v_sub_u32_e32 v9, v9, v10
	v_cmp_eq_u32_e64 s[2:3], 0, v9
	s_and_b64 s[2:3], s[0:1], s[2:3]
	s_and_saveexec_b64 s[0:1], s[2:3]
	s_cbranch_execz .Lwalk13_s6
	v_lshl_add_u32 v8, v8, 10, v25
	ds_write_b32 v8, v7
.Lwalk13_s6:
	s_or_b64 exec, exec, s[0:1]
	v_fma_f32 v7, v240, v7, v241
	v_add_u32_e32 v227, v227, v6
	global_load_dwordx2 v[240:241], v[244:245], off
	v_lshl_add_u64 v[244:245], v[244:245], 0, v[246:247]
	s_waitcnt vmcnt(7)
	v_subrev_u32_e32 v9, s20, v227
	v_sub_u32_e32 v10, 0, v9
	v_max_i32_e32 v10, v9, v10
	v_mul_hi_u32 v12, v10, v26
	v_mul_lo_u32 v13, v12, s13
	v_sub_u32_e32 v10, v10, v13
	v_add_u32_e32 v13, 1, v12
	v_cmp_le_u32_e64 s[2:3], s13, v10
	v_ashrrev_i32_e32 v8, 31, v9
	v_xor_b32_e32 v8, s14, v8
	v_cndmask_b32_e64 v12, v12, v13, s[2:3]
	v_subrev_u32_e32 v13, s13, v10
	v_cndmask_b32_e64 v10, v10, v13, s[2:3]
	v_add_u32_e32 v13, 1, v12
	v_cmp_le_u32_e64 s[2:3], s13, v10
	v_cmp_lt_i32_e64 s[0:1], -1, v9
	s_nop 0
	v_cndmask_b32_e64 v10, v12, v13, s[2:3]
	v_xor_b32_e32 v10, v10, v8
	v_sub_u32_e32 v8, v10, v8
	v_mul_lo_u32 v10, v8, s21
	v_sub_u32_e32 v9, v9, v10
	v_cmp_eq_u32_e64 s[2:3], 0, v9
	s_and_b64 s[2:3], s[0:1], s[2:3]
	s_and_saveexec_b64 s[0:1], s[2:3]
	s_cbranch_execz .Lwalk13_s7
	v_lshl_add_u32 v8, v8, 10, v25
	ds_write_b32 v8, v7
.Lwalk13_s7:
	s_or_b64 exec, exec, s[0:1]
	v_fma_f32 v7, v242, v7, v243
	v_add_u32_e32 v227, v227, v6
	global_load_dwordx2 v[242:243], v[244:245], off
	v_lshl_add_u64 v[244:245], v[244:245], 0, v[246:247]
	s_sub_u32 s5, s5, 1
	s_cmp_lg_u32 s5, 0
	s_cbranch_scc1 .Lwalk13
	s_waitcnt vmcnt(0)
	s_branch .LBB0_1566
